# attention step decode: 9 scalar-compare to 0/1 conversions done with s_cselect_b32 instead of mask, v_cndmask and v_readfirstlane round trips
# baseline (speedup 1.0000x reference)
; #define AT_SU(s_) (2 * AT_P((s_) >> 1) + ((s_) & 1))
; #define AT_OK(s_) ((s_) < ns && AT_P((s_) >> 1) < NP)
; #define AT_SU(s_) (2 * AT_P((s_) >> 1) + ((s_) & 1))
; __device__ __forceinline__ void attn_group_mfma5(const bf16* QK, const float* bias2g, int ldil, int first, bf16* OACC, float* LSE, LAS unsigned char* lds, const int tid, const int bid, const int G) {
;     ...
;         if (!AT_OK(s)) break;
;         const bool more = AT_OK(s + 1);
;         if (more) { bv = AT_BIAS(AT_SU(s + 1)); AT_DMA(AT_SU(s + 1), (s + 1) & 1); }
;         const int su = AT_SU(s), q4 = su & nq4m, rr = (su >> lq4) & dilm, h = (su >> 4) & 15, b = su >> 8;
.LBB0_190:
	s_bfe_u32 s36, s0, 0x20001
	s_cmp_lt_u32 s0, 8
	s_cselect_b64 s[8:9], -1, 0
	s_cselect_b32 s8, 1, 0
	s_or_b32 s8, s51, s8
	s_lshl_b32 s8, s8, 7
	s_or_b32 s8, s8, s36
	s_or_b32 s36, s8, s56
	s_cmpk_gt_i32 s36, 0x7ff
	s_mov_b64 s[8:9], -1
	s_cbranch_scc1 .LBB0_185

; #define AT_SU(s_) (2 * AT_P((s_) >> 1) + ((s_) & 1))
; #define AT_OK(s_) ((s_) < ns && AT_P((s_) >> 1) < NP)
; #define AT_SU(s_) (2 * AT_P((s_) >> 1) + ((s_) & 1))
; __device__ __forceinline__ void attn_group_mfma5(const bf16* QK, const float* bias2g, int ldil, int first, bf16* OACC, float* LSE, LAS unsigned char* lds, const int tid, const int bid, const int G) {
;     ...
;         if (!AT_OK(s)) break;
;         const bool more = AT_OK(s + 1);
;         if (more) { bv = AT_BIAS(AT_SU(s + 1)); AT_DMA(AT_SU(s + 1), (s + 1) & 1); }
.LBB0_194:
	s_andn2_b64 vcc, exec, s[8:9]
	s_cbranch_vccnz .LBB0_196
	s_bfe_u32 s36, s77, 0x20001
	s_cmp_lt_u32 s0, 7
	s_cselect_b64 s[8:9], -1, 0
	s_cselect_b32 s8, 1, 0
	s_or_b32 s8, s51, s8
	s_lshl_b32 s8, s8, 7
	s_or_b32 s8, s8, s36
	s_or_b32 s36, s8, s56

; #define AT_SU(s_) (2 * AT_P((s_) >> 1) + ((s_) & 1))
; #define AT_SU(s_) (2 * AT_P((s_) >> 1) + ((s_) & 1))
; __device__ __forceinline__ void attn_group_mfma5(const bf16* QK, const float* bias2g, int ldil, int first, bf16* OACC, float* LSE, LAS unsigned char* lds, const int tid, const int bid, const int G) {
;     ...
;         if (more) { bv = AT_BIAS(AT_SU(s + 1)); AT_DMA(AT_SU(s + 1), (s + 1) & 1); }
;         const int su = AT_SU(s), q4 = su & nq4m, rr = (su >> lq4) & dilm, h = (su >> 4) & 15, b = su >> 8;
.LBB0_205:
	s_bfe_u32 s42, s77, 0x20001
	s_cmp_lt_u32 s0, 7
	s_cselect_b64 s[36:37], -1, 0
	s_cselect_b32 s36, 1, 0
	s_or_b32 s36, s51, s36
	s_lshl_b32 s36, s36, 7
	s_or_b32 s36, s36, s42
	s_or_b32 s60, s36, s56

; #define AT_SU(s_) (2 * AT_P((s_) >> 1) + ((s_) & 1))
; #define AT_SU(s_) (2 * AT_P((s_) >> 1) + ((s_) & 1))
; __device__ __forceinline__ void attn_group_mfma5(const bf16* QK, const float* bias2g, int ldil, int first, bf16* OACC, float* LSE, LAS unsigned char* lds, const int tid, const int bid, const int G) {
;     ...
;         const int su = AT_SU(s), q4 = su & nq4m, rr = (su >> lq4) & dilm, h = (su >> 4) & 15, b = su >> 8;
.LBB0_208:
	s_bfe_u32 s1, s0, 0x20001
	s_cmp_lt_u32 s0, 8
	s_cselect_b64 s[36:37], -1, 0
	s_cselect_b32 s36, 1, 0
	s_or_b32 s36, s51, s36
	s_lshl_b32 s36, s36, 7
	s_or_b32 s1, s36, s1
	s_or_b32 s42, s1, s56

; #define AT_SU(s_) (2 * AT_P((s_) >> 1) + ((s_) & 1))
; #define AT_FETCH_Q(su_) do { const int su__ = (su_); const bf16* qp_ = QK + ((((size_t)((su__ >> 8) * 16 + ((su__ >> 4) & 15)) << ldil) | ((su__ >> lq4) & dilm)) * Ls + ((su__ & nq4m) * 128 + 16 * wq + n)) * 64 + 8 * kq; \
;         qf[0] = *(const bf16x8s*)qp_; qf[1] = *(const bf16x8s*)(qp_ + 32); } while (0)
; #define AT_SU(s_) (2 * AT_P((s_) >> 1) + ((s_) & 1))
; #define AT_FETCH_Q(su_) do { const int su__ = (su_); const bf16* qp_ = QK + ((((size_t)((su__ >> 8) * 16 + ((su__ >> 4) & 15)) << ldil) | ((su__ >> lq4) & dilm)) * Ls + ((su__ & nq4m) * 128 + 16 * wq + n)) * 64 + 8 * kq; \
;         qf[0] = *(const bf16x8s*)qp_; qf[1] = *(const bf16x8s*)(qp_ + 32); tick += 2; } while (0)
; __device__ __forceinline__ void attn_group_mfma5(const bf16* QK, const float* bias2g, int ldil, int first, bf16* OACC, float* LSE, LAS unsigned char* lds, const int tid, const int bid, const int G) {
;     ...
;         if (more) AT_FETCH_Q(AT_SU(s + 1));
.LBB0_212:
	s_andn2_b64 vcc, exec, s[8:9]
	s_cbranch_vccnz .LBB0_214
	s_bfe_u32 s37, s77, 0x20001
	s_cmp_lt_u32 s0, 7
	s_cselect_b64 s[8:9], -1, 0
	s_cselect_b32 s0, 1, 0
	s_or_b32 s0, s51, s0
	s_lshl_b32 s0, s0, 7
	s_or_b32 s0, s0, s37
	s_or_b32 s37, s0, s56

; __device__ __forceinline__ void attn_group_ring(const bf16* QK, const float* bias2g, int ldil, int first, bf16* OACC, float* LSE, LAS unsigned char* lds, const int tid, const int bid, const int G) {
;     ...
;         const int rn = s / R, jn = s - rn * R, a = rn * RH + jn;
;         if (iss <= a + 3 && iss < NH) { AT_DMAH(iss); ++iss; }
;         if (iss <= a + 3 && iss < NH) { AT_DMAH(iss); ++iss; }
.LBB0_234:
	s_lshr_b32 s0, s87, s50
	s_lshl_b32 s1, s0, s50
	s_mul_i32 s0, s0, s56
	s_sub_i32 s0, s0, s1
	s_add_i32 s1, s87, s0
	s_add_i32 s1, s1, 3
	s_cmp_le_i32 s16, s1
	s_cselect_b64 s[4:5], -1, 0
	s_cmp_lt_i32 s16, s57
	s_cselect_b64 s[10:11], -1, 0
	s_and_b64 s[4:5], s[4:5], s[10:11]
	s_andn2_b64 vcc, exec, s[4:5]
	s_cbranch_vccnz .LBB0_236
	s_abs_i32 s5, s16
	s_mul_hi_u32 s10, s5, s92
	s_mul_i32 s11, s10, s56
	s_sub_i32 s5, s5, s11
	s_ashr_i32 s4, s16, 31
	s_add_i32 s11, s10, 1
	s_sub_i32 s42, s5, s56
	s_cmp_ge_u32 s5, s56
	s_cselect_b32 s10, s11, s10
	s_cselect_b32 s5, s42, s5
	s_add_i32 s11, s10, 1
	s_cmp_ge_u32 s5, s56
	s_cselect_b32 s5, s11, s10
	s_xor_b32 s5, s5, s4
	s_sub_i32 s4, s5, s4
	s_mul_i32 s5, s4, s56
	s_sub_i32 s5, s16, s5
	s_cmp_eq_u32 s5, s51
	s_cselect_b32 s10, 64, 0xffffffc0
	s_and_b32 s11, s5, 1
	s_cmp_eq_u32 s5, s51
	s_cselect_b32 s5, s60, s5
	s_cselect_b32 s11, 1, s11
	s_lshl_b32 s4, s4, s50
	s_add_i32 s5, s5, s4
	s_bfe_u32 s42, s5, 0x20001
	s_cmp_lt_u32 s5, 8
	s_cselect_b64 s[4:5], -1, 0
	s_cselect_b32 s4, 1, 0
	v_mov_b32_e32 v14, v66
	s_or_b32 s4, s49, s4
	s_lshl_b32 s5, s4, 7
	s_or_b32 s5, s5, s42
	s_or_b32 s5, s5, s45
	s_lshl_b32 s5, s5, 1
	s_or_b32 s5, s5, s11
	s_and_b32 s11, s5, s47
	s_ashr_i32 s5, s5, s14
	s_lshl_b32 s4, s4, 4
	s_and_b32 s42, s5, s48
	s_lshl_b32 s5, s11, 7
	s_or_b32 s4, s4, s46
	s_add_i32 s10, s5, s10
	s_ashr_i32 s5, s4, 31
	s_lshl_b64 s[4:5], s[4:5], s43
	s_and_b32 s11, s16, 3
	v_ashrrev_i32_e32 v15, 3, v14
	s_or_b32 s4, s4, s42
	s_add_i32 s42, s10, s37
	s_lshl_b32 vcc_lo, s11, 15
	v_add_u32_e32 v0, s42, v15
	s_add_i32 s70, vcc_lo, 0
	v_min_i32_e32 v1, s15, v0
	v_cmp_lt_i32_e32 vcc, -1, v0
	s_lshl_b64 s[4:5], s[4:5], s33
	s_mov_b64 s[20:21], 0x8000000
	v_cndmask_b32_e32 v2, 0, v1, vcc
	v_lshl_add_u64 v[0:1], s[4:5], 0, v[2:3]
	v_lshrrev_b32_e32 v2, 1, v15
	v_xor_b32_e32 v2, v2, v14
	v_lshlrev_b64 v[0:1], 7, v[0:1]
	v_lshlrev_b32_e32 v2, 4, v2
	v_lshl_add_u64 v[0:1], s[80:81], 0, v[0:1]
	v_and_b32_e32 v2, 0x70, v2
	v_lshl_add_u64 v[0:1], v[0:1], 0, v[2:3]
	s_mov_b64 s[22:23], 0x4000000
	s_add_i32 s42, s70, s36
	v_lshl_add_u64 v[12:13], v[0:1], 0, s[20:21]
	v_lshl_add_u64 v[0:1], v[0:1], 0, s[22:23]
	s_mov_b32 m0, s42
	s_add_i32 s10, s10, s39
	global_load_lds_dwordx4 v[0:1], off nt
	v_add_u32_e32 v0, s10, v15
	v_min_i32_e32 v1, s15, v0
	v_cmp_lt_i32_e32 vcc, -1, v0
	s_add_i32 m0, s70, s44
	s_add_i32 s41, s41, 4
	v_cndmask_b32_e32 v2, 0, v1, vcc
	v_lshl_add_u64 v[0:1], s[4:5], 0, v[2:3]
	v_add_u32_e32 v2, s39, v15
	v_lshrrev_b32_e32 v2, 1, v2
	v_xor_b32_e32 v2, v2, v14
	v_lshlrev_b64 v[0:1], 7, v[0:1]
	v_lshlrev_b32_e32 v2, 4, v2
	v_lshl_add_u64 v[0:1], s[80:81], 0, v[0:1]
	v_and_b32_e32 v2, 0x70, v2
	v_lshl_add_u64 v[0:1], v[0:1], 0, v[2:3]
	v_lshl_add_u64 v[14:15], v[0:1], 0, s[20:21]
	v_lshl_add_u64 v[0:1], v[0:1], 0, s[22:23]
	global_load_lds_dwordx4 v[0:1], off nt
	s_add_i32 m0, s42, 0x4000
	s_nop 0
	global_load_lds_dwordx4 v[12:13], off nt
	s_add_i32 m0, s42, 0x4400
	s_cmp_eq_u32 s11, 3
	global_load_lds_dwordx4 v[14:15], off nt
	s_cselect_b32 s55, s41, s55
	s_cmp_eq_u32 s11, 2
	s_cselect_b32 s54, s41, s54
	s_cmp_eq_u32 s11, 1
	s_cselect_b32 s53, s41, s53
	s_cmp_eq_u32 s11, 0
	s_cselect_b32 s52, s41, s52
	s_add_i32 s16, s16, 1
.LBB0_236:
	s_cmp_le_i32 s16, s1
	s_cselect_b64 s[4:5], -1, 0
	s_cmp_lt_i32 s16, s57
	s_cselect_b64 s[10:11], -1, 0
	s_and_b64 s[4:5], s[4:5], s[10:11]
	s_andn2_b64 vcc, exec, s[4:5]
	s_cbranch_vccnz .LBB0_238
	s_abs_i32 s4, s16
	s_mul_hi_u32 s5, s4, s92
	s_mul_i32 s10, s5, s56
	s_sub_i32 s4, s4, s10
	s_ashr_i32 s1, s16, 31
	s_add_i32 s10, s5, 1
	s_sub_i32 s11, s4, s56
	s_cmp_ge_u32 s4, s56
	s_cselect_b32 s5, s10, s5
	s_cselect_b32 s4, s11, s4
	s_add_i32 s10, s5, 1
	s_cmp_ge_u32 s4, s56
	s_cselect_b32 s4, s10, s5
	s_xor_b32 s4, s4, s1
	s_sub_i32 s1, s4, s1
	s_mul_i32 s4, s1, s56
	s_sub_i32 s4, s16, s4
	s_cmp_eq_u32 s4, s51
	s_cselect_b32 s10, 64, 0xffffffc0
	s_and_b32 s5, s4, 1
	s_cmp_eq_u32 s4, s51
	s_cselect_b32 s4, s60, s4
	s_cselect_b32 s11, 1, s5
	s_lshl_b32 s1, s1, s50
	s_add_i32 s4, s4, s1
	s_bfe_u32 s1, s4, 0x20001
	s_cmp_lt_u32 s4, 8
	s_cselect_b64 s[4:5], -1, 0
	s_cselect_b32 s4, 1, 0
	v_mov_b32_e32 v14, v66
	s_or_b32 s4, s49, s4
	s_lshl_b32 s5, s4, 7
	s_or_b32 s1, s5, s1
	s_or_b32 s1, s1, s45
	s_lshl_b32 s1, s1, 1
	s_or_b32 s1, s1, s11
	s_and_b32 s5, s1, s47
	s_lshl_b32 s4, s4, 4
	s_lshl_b32 s5, s5, 7
	s_or_b32 s4, s4, s46
	s_ashr_i32 s1, s1, s14
	s_add_i32 s10, s5, s10
	s_ashr_i32 s5, s4, 31
	s_and_b32 s1, s1, s48
	s_lshl_b64 s[4:5], s[4:5], s43
	s_or_b32 s4, s4, s1
	v_ashrrev_i32_e32 v15, 3, v14
	s_add_i32 s1, s10, s37
	v_add_u32_e32 v0, s1, v15
	v_min_i32_e32 v1, s15, v0
	v_cmp_lt_i32_e32 vcc, -1, v0
	s_lshl_b64 s[4:5], s[4:5], s33
	s_and_b32 s11, s16, 3
	v_cndmask_b32_e32 v2, 0, v1, vcc
	v_lshl_add_u64 v[0:1], s[4:5], 0, v[2:3]
	v_lshrrev_b32_e32 v2, 1, v15
	v_xor_b32_e32 v2, v2, v14
	s_lshl_b32 s42, s11, 15
	v_lshlrev_b64 v[0:1], 7, v[0:1]
	v_lshlrev_b32_e32 v2, 4, v2
	s_add_i32 s42, s42, 0
	v_lshl_add_u64 v[0:1], s[80:81], 0, v[0:1]
	v_and_b32_e32 v2, 0x70, v2
	v_lshl_add_u64 v[0:1], v[0:1], 0, v[2:3]
	s_mov_b64 s[20:21], 0x8000000
	s_mov_b64 s[22:23], 0x4000000
	s_add_i32 s1, s42, s36
	v_lshl_add_u64 v[12:13], v[0:1], 0, s[20:21]
	v_lshl_add_u64 v[0:1], v[0:1], 0, s[22:23]
	s_mov_b32 m0, s1
	s_add_i32 s10, s10, s39
	global_load_lds_dwordx4 v[0:1], off nt
	v_add_u32_e32 v0, s10, v15
	v_min_i32_e32 v1, s15, v0
	v_cmp_lt_i32_e32 vcc, -1, v0
	s_add_i32 m0, s42, s44
	s_add_i32 s41, s41, 4
	v_cndmask_b32_e32 v2, 0, v1, vcc
	v_lshl_add_u64 v[0:1], s[4:5], 0, v[2:3]
	v_add_u32_e32 v2, s39, v15
	v_lshrrev_b32_e32 v2, 1, v2
	v_xor_b32_e32 v2, v2, v14
	v_lshlrev_b64 v[0:1], 7, v[0:1]
	v_lshlrev_b32_e32 v2, 4, v2
	v_lshl_add_u64 v[0:1], s[80:81], 0, v[0:1]
	v_and_b32_e32 v2, 0x70, v2
	v_lshl_add_u64 v[0:1], v[0:1], 0, v[2:3]
	v_lshl_add_u64 v[14:15], v[0:1], 0, s[20:21]
	v_lshl_add_u64 v[0:1], v[0:1], 0, s[22:23]
	global_load_lds_dwordx4 v[0:1], off nt
	s_add_i32 m0, s1, 0x4000
	s_nop 0
	global_load_lds_dwordx4 v[12:13], off nt
	s_add_i32 m0, s1, 0x4400
	s_cmp_eq_u32 s11, 3
	global_load_lds_dwordx4 v[14:15], off nt
	s_cselect_b32 s55, s41, s55
	s_cmp_eq_u32 s11, 2
	s_cselect_b32 s54, s41, s54
	s_cmp_eq_u32 s11, 1
	s_cselect_b32 s53, s41, s53
	s_cmp_eq_u32 s11, 0
	s_cselect_b32 s52, s41, s52
	s_add_i32 s16, s16, 1
; #define LAS __attribute__((address_space(3)))
; #define AT_SU(s_) (2 * AT_P((s_) >> 1) + ((s_) & 1))
; #define AT_FETCH_Q(su_) do { const int su__ = (su_); const bf16* qp_ = QK + ((((size_t)((su__ >> 8) * 16 + ((su__ >> 4) & 15)) << ldil) | ((su__ >> lq4) & dilm)) * Ls + ((su__ & nq4m) * 128 + 16 * wq + n)) * 64 + 8 * kq; \
;         qf[0] = *(const bf16x8s*)qp_; qf[1] = *(const bf16x8s*)(qp_ + 32); } while (0)
; #define AT_SU(s_) (2 * AT_P((s_) >> 1) + ((s_) & 1))
; #define AT_FETCH_Q(su_) do { const int su__ = (su_); const bf16* qp_ = QK + ((((size_t)((su__ >> 8) * 16 + ((su__ >> 4) & 15)) << ldil) | ((su__ >> lq4) & dilm)) * Ls + ((su__ & nq4m) * 128 + 16 * wq + n)) * 64 + 8 * kq; \
;         qf[0] = *(const bf16x8s*)qp_; qf[1] = *(const bf16x8s*)(qp_ + 32); tick += 2; } while (0)
; __device__ __forceinline__ void attn_group_ring(const bf16* QK, const float* bias2g, int ldil, int first, bf16* OACC, float* LSE, LAS unsigned char* lds, const int tid, const int bid, const int G) {
;     ...
; #pragma unroll
;         for (int ks = 0; ks < 2; ++ks)
; #pragma unroll
;             for (int kb = 0; kb < 9; ++kb) { const int wrow = 16 * (wq + kb);
;                 const LAS unsigned char* kp = lds + ((a + (wrow >> 7)) & 3) * 32768 + ((wrow & 127) + n) * 128 + (((4 * ks + kq) ^ fl) * 16);
;                 S[kb] = __builtin_amdgcn_mfma_f32_16x16x32_bf16(*(const LAS bf16x8s*)kp, qf[ks], S[kb], 0, 0, 0); }
;         __builtin_amdgcn_sched_barrier(0);
;         if (more) AT_FETCH_Q(AT_SU(s + 1));
;         float lold = 0.f; v2u xo[4];
;         if (!first) { lold = LSE[rowq * 16 + h];
; #pragma unroll
;             for (int db = 0; db < 4; ++db) xo[db] = *(const v2u*)(OACC + rowq * D + h * 64 + 16 * db + 4 * kq); }
.LBB0_238:
	s_add_i32 s42, s87, 1
	s_cmp_lt_u32 s87, 15
	s_cselect_b64 s[10:11], -1, 0
	s_add_i32 s1, s62, s87
	s_add_i32 s1, s1, s0
	s_add_i32 s71, s73, s87
	s_lshl_b32 s1, s1, 15
	s_add_i32 s71, s71, s0
	s_and_b32 s1, s1, 0x18000
	s_lshl_b32 s71, s71, 15
	v_add_u32_e32 v0, s1, v68
	s_and_b32 s1, s71, 0x18000
	v_add_u32_e32 v89, s1, v74
	s_add_i32 s1, s76, s87
	s_add_i32 s1, s1, s0
	s_add_i32 s4, s63, s87
	s_lshl_b32 s1, s1, 15
	s_add_i32 s4, s4, s0
	s_and_b32 s1, s1, 0x18000
	s_lshl_b32 s4, s4, 15
	s_add_i32 s71, s74, s87
	v_add_u32_e32 v92, s1, v77
	s_and_b32 s4, s4, 0x18000
	v_add_u32_e32 v1, v0, v69
	s_add_i32 s71, s71, s0
	v_add_u32_e32 v40, v92, v69
	ds_read_b128 v[12:15], v1
	ds_read_b128 v[40:43], v40
	v_add_u32_e32 v1, s4, v71
	s_lshl_b32 s4, s71, 15
	s_and_b32 s4, s4, 0x18000
	v_add_u32_e32 v90, s4, v75
	v_add_u32_e32 v32, v90, v69
	ds_read_b128 v[32:35], v32
	s_add_i32 s1, s77, s87
	s_add_i32 s1, s1, s0
	s_lshl_b32 s1, s1, 15
	s_and_b32 s1, s1, 0x18000
	v_add_u32_e32 v93, s1, v67
	s_waitcnt lgkmcnt(0)
	v_mfma_f32_16x16x32_bf16 v[52:55], v[32:35], v[4:7], 0
	v_add_u32_e32 v32, v93, v69
	ds_read_b128 v[32:35], v32
	v_add_u32_e32 v2, v1, v69
	v_add_u32_e32 v0, v0, v78
	ds_read_b128 v[16:19], v2
	s_waitcnt lgkmcnt(0)
	v_mfma_f32_16x16x32_bf16 v[84:87], v[32:35], v[4:7], 0
	ds_read_b128 v[32:35], v0
	s_add_i32 s5, s68, s87
	s_add_i32 s5, s5, s0
	s_lshl_b32 s5, s5, 15
	v_mfma_f32_16x16x32_bf16 v[12:15], v[12:15], v[4:7], 0
	s_and_b32 s5, s5, 0x18000
	v_add_u32_e32 v2, s5, v72
	v_add_u32_e32 v20, v2, v69
	v_add_u32_e32 v0, v1, v78
	ds_read_b128 v[20:23], v20
	s_waitcnt lgkmcnt(0)
	v_mfma_f32_16x16x32_bf16 v[44:47], v[32:35], v[8:11], v[12:15]
	s_add_i32 s70, s72, s87
	s_add_i32 s5, s75, s87
	s_add_i32 s70, s70, s0
	ds_read_b128 v[12:15], v0
	s_add_i32 s5, s5, s0
	s_lshl_b32 s70, s70, 15
	v_mfma_f32_16x16x32_bf16 v[16:19], v[16:19], v[4:7], 0
	s_lshl_b32 s5, s5, 15
	s_and_b32 s70, s70, 0x18000
	s_and_b32 s5, s5, 0x18000
	v_add_u32_e32 v88, s70, v73
	v_add_u32_e32 v91, s5, v76
	v_add_u32_e32 v24, v88, v69
	v_add_u32_e32 v36, v91, v69
	v_add_u32_e32 v0, v2, v78
	ds_read_b128 v[24:27], v24
	ds_read_b128 v[36:39], v36
	v_mfma_f32_16x16x32_bf16 v[60:63], v[40:43], v[4:7], 0
	v_add_u32_e32 v28, v89, v69
	ds_read_b128 v[28:31], v28
	s_cmp_gt_u32 s87, 14
	s_waitcnt lgkmcnt(0)
	v_mfma_f32_16x16x32_bf16 v[40:43], v[12:15], v[8:11], v[16:19]
	ds_read_b128 v[12:15], v0
	v_add_u32_e32 v0, v88, v78
	v_mfma_f32_16x16x32_bf16 v[20:23], v[20:23], v[4:7], 0
	v_mfma_f32_16x16x32_bf16 v[56:59], v[36:39], v[4:7], 0
	s_waitcnt lgkmcnt(0)
	v_mfma_f32_16x16x32_bf16 v[36:39], v[12:15], v[8:11], v[20:23]
	ds_read_b128 v[12:15], v0
	v_add_u32_e32 v0, v89, v78
	v_mfma_f32_16x16x32_bf16 v[24:27], v[24:27], v[4:7], 0
	s_waitcnt lgkmcnt(0)
	v_mfma_f32_16x16x32_bf16 v[32:35], v[12:15], v[8:11], v[24:27]
	ds_read_b128 v[12:15], v0
	v_add_u32_e32 v0, v90, v78
	v_mfma_f32_16x16x32_bf16 v[28:31], v[28:31], v[4:7], 0
	s_waitcnt lgkmcnt(0)
	v_mfma_f32_16x16x32_bf16 v[28:31], v[12:15], v[8:11], v[28:31]
	ds_read_b128 v[12:15], v0
	v_add_u32_e32 v0, v91, v78
	s_waitcnt lgkmcnt(0)
	v_mfma_f32_16x16x32_bf16 v[24:27], v[12:15], v[8:11], v[52:55]
	ds_read_b128 v[12:15], v0
	v_add_u32_e32 v0, v92, v78
	s_waitcnt lgkmcnt(0)
	v_mfma_f32_16x16x32_bf16 v[20:23], v[12:15], v[8:11], v[56:59]
	ds_read_b128 v[12:15], v0
	v_add_u32_e32 v0, v93, v78
	s_waitcnt lgkmcnt(0)
	v_mfma_f32_16x16x32_bf16 v[16:19], v[12:15], v[8:11], v[60:63]
	ds_read_b128 v[12:15], v0
	s_waitcnt lgkmcnt(0)
	v_mfma_f32_16x16x32_bf16 v[12:15], v[12:15], v[8:11], v[84:87]
	s_cbranch_scc1 .LBB0_240
	s_bfe_u32 s1, s42, 0x20001
	s_cmp_lt_u32 s87, 7
	s_cselect_b64 s[4:5], -1, 0
	s_cselect_b32 s4, 1, 0
	s_add_i32 s41, s41, 2
	s_or_b32 s4, s49, s4
	s_lshl_b32 s5, s4, 7
	s_or_b32 s1, s5, s1
	s_or_b32 s1, s1, s45
	s_lshl_b32 s1, s1, 1
	s_and_b32 s5, s42, 1
	s_lshl_b32 s4, s4, 4
	s_or_b32 s1, s1, s5
	s_or_b32 s4, s4, s46
	s_ashr_i32 s5, s4, 31
	s_ashr_i32 s70, s1, s14
	s_lshl_b64 s[4:5], s[4:5], s43
	s_and_b32 s70, s70, s48
	s_and_b32 s1, s1, s47
	s_or_b32 s4, s4, s70
	v_lshl_add_u32 v0, s1, 7, v64
	s_lshl_b64 s[4:5], s[4:5], s33
	v_ashrrev_i32_e32 v1, 31, v0
	v_lshl_add_u64 v[0:1], s[4:5], 0, v[0:1]
	v_lshlrev_b64 v[0:1], 7, v[0:1]
	v_lshl_add_u64 v[0:1], v[48:49], 0, v[0:1]
	global_load_dwordx4 v[4:7], v[0:1], off
	global_load_dwordx4 v[8:11], v[0:1], off offset:64
.LBB0_240:
	s_bfe_u32 s1, s87, 0x20001
	s_cmp_lt_u32 s87, 8
	s_cselect_b64 s[4:5], -1, 0
	s_cselect_b32 s4, 1, 0
	v_cndmask_b32_e64 v2, 0, 1, s[6:7]
	s_or_b32 s4, s49, s4
	s_lshl_b32 s5, s4, 7
	s_or_b32 s1, s5, s1
	s_or_b32 s1, s1, s45
	s_lshl_b32 s1, s1, 1
	s_and_b32 s5, s87, 1
	s_or_b32 s1, s1, s5
	s_and_b32 s70, s1, s47
	s_ashr_i32 s1, s1, s14
	s_and_b32 s71, s1, s48
	s_lshl_b32 s1, s70, 7
	s_ashr_i32 s5, s4, 31
	v_add_u32_e32 v0, s1, v64
	s_lshl_b64 s[4:5], s[4:5], 11
	v_ashrrev_i32_e32 v1, 31, v0
	s_or_b32 s4, s4, s71
	v_lshlrev_b64 v[0:1], s43, v[0:1]
	v_lshl_add_u64 v[0:1], s[4:5], 0, v[0:1]
	v_lshlrev_b64 v[52:53], 6, v[0:1]
	v_lshlrev_b64 v[0:1], 11, v[0:1]
	v_cmp_ne_u32_e64 s[4:5], 1, v2
	s_andn2_b64 vcc, exec, s[6:7]
	v_lshl_add_u64 v[60:61], s[8:9], 0, v[52:53]
	v_lshl_add_u64 v[52:53], v[50:51], 0, v[0:1]
	s_cbranch_vccnz .LBB0_242
	global_load_dword v84, v[60:61], off
	global_load_dwordx2 v[62:63], v[52:53], off
	global_load_dwordx2 v[58:59], v[52:53], off offset:32
	global_load_dwordx2 v[56:57], v[52:53], off offset:64
	global_load_dwordx2 v[54:55], v[52:53], off offset:96
	s_branch .LBB0_243
